# v45 + GQA step heads MFMA-only: finish-softmax VALU spread over QK^T gaps 7..16 only (first six gaps left free)
# baseline (speedup 1.0000x reference)
.LBB0_881:
	ds_read_b128 v[96:99], v216 offset:49152
	ds_read_b128 v[100:103], v216 offset:57344
	ds_read_b128 v[178:181], v218 offset:49152
	ds_read_b128 v[182:185], v218 offset:57344
	ds_read_b128 v[240:243], v219 offset:49152
	ds_read_b128 v[244:247], v219 offset:57344
	s_waitcnt lgkmcnt(5)
	v_mfma_f32_32x32x16_bf16 v[112:127], v[96:99], v[138:141], 0
	s_waitcnt lgkmcnt(4)
	v_mfma_f32_32x32x16_bf16 v[96:111], v[100:103], v[138:141], 0
	s_waitcnt lgkmcnt(3)
	v_mfma_f32_32x32x16_bf16 v[112:127], v[178:181], v[154:157], v[112:127]
	s_waitcnt lgkmcnt(2)
	v_mfma_f32_32x32x16_bf16 v[96:111], v[182:185], v[154:157], v[96:111]
	ds_read_b128 v[178:181], v220 offset:49152
	ds_read_b128 v[182:185], v220 offset:57344
	s_waitcnt lgkmcnt(3)
	v_mfma_f32_32x32x16_bf16 v[112:127], v[240:243], v[158:161], v[112:127]
	s_waitcnt lgkmcnt(2)
	v_mfma_f32_32x32x16_bf16 v[96:111], v[244:247], v[158:161], v[96:111]
	ds_read_b128 v[240:243], v221 offset:49152
	ds_read_b128 v[244:247], v221 offset:57344
	v_add_f32_e32 v88, v64, v65
	v_add_f32_e32 v89, v72, v73
	v_add_f32_e32 v90, v80, v81
	v_add_f32_e32 v91, v194, v195
	v_add_f32_e32 v88, v66, v88
	v_add_f32_e32 v89, v74, v89
	s_waitcnt lgkmcnt(3)
	v_mfma_f32_32x32x16_bf16 v[112:127], v[178:181], v[150:153], v[112:127]
	v_add_f32_e32 v90, v82, v90
	v_add_f32_e32 v91, v196, v91
	v_add_f32_e32 v88, v67, v88
	v_add_f32_e32 v89, v75, v89
	v_add_f32_e32 v90, v83, v90
	s_waitcnt lgkmcnt(2)
	v_mfma_f32_32x32x16_bf16 v[96:111], v[182:185], v[150:153], v[96:111]
	ds_read_b128 v[178:181], v222 offset:49152
	ds_read_b128 v[182:185], v222 offset:57344
	v_add_f32_e32 v91, v197, v91
	v_add_f32_e32 v88, v68, v88
	v_add_f32_e32 v89, v76, v89
	v_add_f32_e32 v90, v84, v90
	v_add_f32_e32 v91, v92, v91
	v_add_f32_e32 v88, v69, v88
	s_waitcnt lgkmcnt(3)
	v_mfma_f32_32x32x16_bf16 v[112:127], v[240:243], v[146:149], v[112:127]
	v_add_f32_e32 v89, v77, v89
	v_add_f32_e32 v90, v85, v90
	v_add_f32_e32 v91, v93, v91
	v_add_f32_e32 v88, v70, v88
	v_add_f32_e32 v89, v78, v89
	v_add_f32_e32 v90, v86, v90
	s_waitcnt lgkmcnt(2)
	v_mfma_f32_32x32x16_bf16 v[96:111], v[244:247], v[146:149], v[96:111]
	ds_read_b128 v[240:243], v224 offset:49152
	ds_read_b128 v[244:247], v224 offset:57344
	v_add_f32_e32 v91, v94, v91
	v_add_f32_e32 v88, v71, v88
	v_add_f32_e32 v89, v79, v89
	v_add_f32_e32 v90, v87, v90
	v_add_f32_e32 v91, v95, v91
	s_waitcnt lgkmcnt(3)
	v_mfma_f32_32x32x16_bf16 v[112:127], v[178:181], v[142:145], v[112:127]
	v_add_f32_e32 v88, v89, v88
	v_add_f32_e32 v89, v91, v90
	v_add_f32_e32 v227, v88, v89
	v_mov_b32_e32 v228, v227
	v_cvt_pk_bf16_f32 v88, v64, v65
	v_cvt_pk_bf16_f32 v89, v66, v67
	s_waitcnt lgkmcnt(2)
	v_mfma_f32_32x32x16_bf16 v[96:111], v[182:185], v[142:145], v[96:111]
	ds_read_b128 v[178:181], v223 offset:49152
	ds_read_b128 v[182:185], v223 offset:57344
	v_cvt_pk_bf16_f32 v90, v68, v69
	v_cvt_pk_bf16_f32 v91, v70, v71
	v_permlane32_swap_b32_e32 v227, v228
	v_cvt_pk_bf16_f32 v72, v72, v73
	s_waitcnt lgkmcnt(3)
	v_mfma_f32_32x32x16_bf16 v[112:127], v[240:243], v[134:137], v[112:127]
	v_cvt_pk_bf16_f32 v73, v74, v75
	v_cvt_pk_bf16_f32 v74, v76, v77
	v_cvt_pk_bf16_f32 v75, v78, v79
	v_cvt_pk_bf16_f32 v64, v80, v81
	v_cvt_pk_bf16_f32 v65, v82, v83
	v_cvt_pk_bf16_f32 v66, v84, v85
	s_waitcnt lgkmcnt(2)
	v_mfma_f32_32x32x16_bf16 v[96:111], v[244:247], v[134:137], v[96:111]
	v_cvt_pk_bf16_f32 v67, v86, v87
	v_cvt_pk_bf16_f32 v68, v194, v195
	v_cvt_pk_bf16_f32 v69, v196, v197
	v_cvt_pk_bf16_f32 v70, v92, v93
	v_cvt_pk_bf16_f32 v71, v94, v95
	s_waitcnt lgkmcnt(1)
	v_mfma_f32_32x32x16_bf16 v[112:127], v[178:181], v[130:133], v[112:127]
	s_waitcnt lgkmcnt(0)
	v_mfma_f32_32x32x16_bf16 v[96:111], v[182:185], v[130:133], v[96:111]
	s_add_i32 s2, s39, -1
	s_mul_i32 s2, s2, s62
	s_lshl_b32 s72, s2, 6
	s_lshl_b64 s[2:3], s[72:73], 1
	s_add_u32 s12, s10, s2
	s_addc_u32 s13, s11, s3
	s_add_u32 s2, s8, s2
	s_addc_u32 s3, s9, s3
	global_load_dwordx4 v[178:181], v128, s[12:13]
	global_load_dwordx4 v[182:185], v198, s[12:13]
	global_load_dwordx4 v[186:189], v128, s[2:3]
	global_load_dwordx4 v[190:193], v198, s[2:3]
	ds_read_b64_tr_b16 v[76:77], v209 offset:0
	ds_read_b64_tr_b16 v[78:79], v209 offset:0x800
	ds_read_b64_tr_b16 v[80:81], v209 offset:0x1000
	ds_read_b64_tr_b16 v[82:83], v209 offset:0x1800
	ds_read_b64_tr_b16 v[84:85], v209 offset:0x2000
	ds_read_b64_tr_b16 v[86:87], v209 offset:0x2800
	ds_read_b64_tr_b16 v[92:93], v209 offset:0x3000
	ds_read_b64_tr_b16 v[94:95], v209 offset:0x3800
	s_waitcnt lgkmcnt(0)
	s_nop 0
	v_mfma_f32_32x32x16_bf16 v[0:15], v[76:79], v[88:91], v[0:15]
	v_mfma_f32_32x32x16_bf16 v[0:15], v[80:83], v[72:75], v[0:15]
	v_mfma_f32_32x32x16_bf16 v[0:15], v[84:87], v[64:67], v[0:15]
	ds_read_b64_tr_b16 v[76:77], v209 offset:0x200
	ds_read_b64_tr_b16 v[78:79], v209 offset:0xa00
	ds_read_b64_tr_b16 v[80:81], v209 offset:0x1200
	v_mfma_f32_32x32x16_bf16 v[0:15], v[92:95], v[68:71], v[0:15]
	ds_read_b64_tr_b16 v[82:83], v209 offset:0x1a00
	ds_read_b64_tr_b16 v[84:85], v209 offset:0x2200
	ds_read_b64_tr_b16 v[86:87], v209 offset:0x2a00
	ds_read_b64_tr_b16 v[92:93], v209 offset:0x3200
	ds_read_b64_tr_b16 v[94:95], v209 offset:0x3a00
	s_waitcnt lgkmcnt(0)
	v_mfma_f32_32x32x16_bf16 v[48:63], v[76:79], v[88:91], v[48:63]
	v_mfma_f32_32x32x16_bf16 v[48:63], v[80:83], v[72:75], v[48:63]
	v_mfma_f32_32x32x16_bf16 v[48:63], v[84:87], v[64:67], v[48:63]
	ds_read_b64_tr_b16 v[76:77], v209 offset:0x400
	ds_read_b64_tr_b16 v[78:79], v209 offset:0xc00
	ds_read_b64_tr_b16 v[80:81], v209 offset:0x1400
	ds_read_b64_tr_b16 v[82:83], v209 offset:0x1c00
	v_mfma_f32_32x32x16_bf16 v[48:63], v[92:95], v[68:71], v[48:63]
	ds_read_b64_tr_b16 v[84:85], v209 offset:0x2400
	ds_read_b64_tr_b16 v[86:87], v209 offset:0x2c00
	ds_read_b64_tr_b16 v[92:93], v209 offset:0x3400
	ds_read_b64_tr_b16 v[94:95], v209 offset:0x3c00
	s_waitcnt lgkmcnt(0)
	v_mfma_f32_32x32x16_bf16 v[32:47], v[76:79], v[88:91], v[32:47]
	ds_read_b64_tr_b16 v[76:77], v209 offset:0x600
	ds_read_b64_tr_b16 v[78:79], v209 offset:0xe00
	v_exp_f32_e32 v234, v104
	v_exp_f32_e32 v235, v105
	v_exp_f32_e32 v236, v106
	v_exp_f32_e32 v237, v107
	v_exp_f32_e32 v238, v108
	v_exp_f32_e32 v239, v109
	v_exp_f32_e32 v231, v110
	v_exp_f32_e32 v249, v111
	v_mfma_f32_32x32x16_bf16 v[32:47], v[80:83], v[72:75], v[32:47]
	v_exp_f32_e32 v80, v112
	v_exp_f32_e32 v81, v113
	v_exp_f32_e32 v82, v114
	v_exp_f32_e32 v83, v115
	v_mfma_f32_32x32x16_bf16 v[32:47], v[84:87], v[64:67], v[32:47]
	v_exp_f32_e32 v84, v116
	v_exp_f32_e32 v85, v117
	v_exp_f32_e32 v86, v118
	v_exp_f32_e32 v87, v119
	v_exp_f32_e32 v112, v96
	v_exp_f32_e32 v113, v97
	v_exp_f32_e32 v114, v98
	v_exp_f32_e32 v115, v99
	v_exp_f32_e32 v116, v100
	v_exp_f32_e32 v117, v101
	v_exp_f32_e32 v118, v102
	v_exp_f32_e32 v119, v103
	v_mfma_f32_32x32x16_bf16 v[32:47], v[92:95], v[68:71], v[32:47]
	ds_read_b64_tr_b16 v[92:93], v209 offset:0x1600
	ds_read_b64_tr_b16 v[94:95], v209 offset:0x1e00
	ds_read_b64_tr_b16 v[96:97], v209 offset:0x2600
	ds_read_b64_tr_b16 v[98:99], v209 offset:0x2e00
	ds_read_b64_tr_b16 v[100:101], v209 offset:0x3600
	ds_read_b64_tr_b16 v[102:103], v209 offset:0x3e00
	s_waitcnt lgkmcnt(0)
	v_mfma_f32_32x32x16_bf16 v[16:31], v[76:79], v[88:91], v[16:31]
	v_exp_f32_e32 v88, v120
	v_exp_f32_e32 v89, v121
	v_exp_f32_e32 v90, v122
	v_exp_f32_e32 v91, v123
	v_mfma_f32_32x32x16_bf16 v[16:31], v[92:95], v[72:75], v[16:31]
	v_exp_f32_e32 v92, v124
	v_exp_f32_e32 v93, v125
	v_exp_f32_e32 v94, v126
	v_exp_f32_e32 v95, v127
	s_barrier
	v_mfma_f32_32x32x16_bf16 v[16:31], v[96:99], v[64:67], v[16:31]
	s_waitcnt vmcnt(4)
	s_waitcnt vmcnt(7)
	ds_write_b128 v212, v[162:165]
	s_waitcnt vmcnt(6)
	ds_write_b128 v213, v[166:169]
	s_waitcnt vmcnt(5)
	ds_write_b128 v214, v[170:173] offset:32768
	s_waitcnt vmcnt(4)
	ds_write_b128 v215, v[174:177] offset:32768
	v_mfma_f32_32x32x16_bf16 v[16:31], v[100:103], v[68:71], v[16:31]
.LBB0_883:
	s_waitcnt lgkmcnt(0)
	s_barrier
	ds_read_b128 v[64:67], v216 offset:32768
	ds_read_b128 v[68:71], v216 offset:40960
	ds_read_b128 v[162:165], v218 offset:32768
	ds_read_b128 v[166:169], v218 offset:40960
	ds_read_b128 v[240:243], v219 offset:32768
	ds_read_b128 v[244:247], v219 offset:40960
	s_waitcnt lgkmcnt(5)
	v_mfma_f32_32x32x16_bf16 v[96:111], v[64:67], v[138:141], 0
	s_waitcnt lgkmcnt(4)
	v_mfma_f32_32x32x16_bf16 v[64:79], v[68:71], v[138:141], 0
	s_waitcnt lgkmcnt(3)
	v_mfma_f32_32x32x16_bf16 v[96:111], v[162:165], v[154:157], v[96:111]
	s_waitcnt lgkmcnt(2)
	v_mfma_f32_32x32x16_bf16 v[64:79], v[166:169], v[154:157], v[64:79]
	ds_read_b128 v[162:165], v220 offset:32768
	ds_read_b128 v[166:169], v220 offset:40960
	s_waitcnt lgkmcnt(3)
	v_mfma_f32_32x32x16_bf16 v[96:111], v[240:243], v[158:161], v[96:111]
	s_waitcnt lgkmcnt(2)
	v_mfma_f32_32x32x16_bf16 v[64:79], v[244:247], v[158:161], v[64:79]
	ds_read_b128 v[240:243], v221 offset:32768
	ds_read_b128 v[244:247], v221 offset:40960
	v_add_f32_e32 v120, v80, v81
	v_add_f32_e32 v121, v88, v89
	v_add_f32_e32 v122, v112, v113
	v_add_f32_e32 v123, v234, v235
	v_add_f32_e32 v120, v82, v120
	v_add_f32_e32 v121, v90, v121
	s_waitcnt lgkmcnt(3)
	v_mfma_f32_32x32x16_bf16 v[96:111], v[162:165], v[150:153], v[96:111]
	v_add_f32_e32 v122, v114, v122
	v_add_f32_e32 v123, v236, v123
	v_add_f32_e32 v120, v83, v120
	v_add_f32_e32 v121, v91, v121
	v_add_f32_e32 v122, v115, v122
	s_waitcnt lgkmcnt(2)
	v_mfma_f32_32x32x16_bf16 v[64:79], v[166:169], v[150:153], v[64:79]
	ds_read_b128 v[162:165], v222 offset:32768
	ds_read_b128 v[166:169], v222 offset:40960
	v_add_f32_e32 v123, v237, v123
	v_add_f32_e32 v120, v84, v120
	v_add_f32_e32 v121, v92, v121
	v_add_f32_e32 v122, v116, v122
	v_add_f32_e32 v123, v238, v123
	v_add_f32_e32 v120, v85, v120
	s_waitcnt lgkmcnt(3)
	v_mfma_f32_32x32x16_bf16 v[96:111], v[240:243], v[146:149], v[96:111]
	v_add_f32_e32 v121, v93, v121
	v_add_f32_e32 v122, v117, v122
	v_add_f32_e32 v123, v239, v123
	v_add_f32_e32 v120, v86, v120
	v_add_f32_e32 v121, v94, v121
	v_add_f32_e32 v122, v118, v122
	s_waitcnt lgkmcnt(2)
	v_mfma_f32_32x32x16_bf16 v[64:79], v[244:247], v[146:149], v[64:79]
	ds_read_b128 v[240:243], v224 offset:32768
	ds_read_b128 v[244:247], v224 offset:40960
	v_add_f32_e32 v123, v231, v123
	v_add_f32_e32 v120, v87, v120
	v_add_f32_e32 v121, v95, v121
	v_add_f32_e32 v122, v119, v122
	v_add_f32_e32 v123, v249, v123
	s_waitcnt lgkmcnt(3)
	v_mfma_f32_32x32x16_bf16 v[96:111], v[162:165], v[142:145], v[96:111]
	v_add_f32_e32 v120, v121, v120
	v_add_f32_e32 v121, v123, v122
	v_add_f32_e32 v229, v120, v121
	v_mov_b32_e32 v233, v229
	s_nop 1
	v_permlane32_swap_b32_e32 v229, v233
	v_cvt_pk_bf16_f32 v124, v80, v81
	s_waitcnt lgkmcnt(2)
	v_mfma_f32_32x32x16_bf16 v[64:79], v[166:169], v[142:145], v[64:79]
	ds_read_b128 v[162:165], v223 offset:32768
	ds_read_b128 v[166:169], v223 offset:40960
	v_cvt_pk_bf16_f32 v125, v82, v83
	v_cvt_pk_bf16_f32 v126, v84, v85
	v_cvt_pk_bf16_f32 v127, v86, v87
	v_cvt_pk_bf16_f32 v120, v88, v89
	v_cvt_pk_bf16_f32 v121, v90, v91
	v_cvt_pk_bf16_f32 v122, v92, v93
	s_waitcnt lgkmcnt(3)
	v_mfma_f32_32x32x16_bf16 v[96:111], v[240:243], v[134:137], v[96:111]
	v_cvt_pk_bf16_f32 v123, v94, v95
	v_cvt_pk_bf16_f32 v112, v112, v113
	v_cvt_pk_bf16_f32 v113, v114, v115
	v_cvt_pk_bf16_f32 v114, v116, v117
	v_cvt_pk_bf16_f32 v115, v118, v119
	v_cvt_pk_bf16_f32 v116, v234, v235
	s_waitcnt lgkmcnt(2)
	v_mfma_f32_32x32x16_bf16 v[64:79], v[244:247], v[134:137], v[64:79]
	v_cvt_pk_bf16_f32 v117, v236, v237
	v_cvt_pk_bf16_f32 v118, v238, v239
	v_cvt_pk_bf16_f32 v119, v231, v249
	s_waitcnt lgkmcnt(1)
	v_mfma_f32_32x32x16_bf16 v[96:111], v[162:165], v[130:133], v[96:111]
	s_waitcnt lgkmcnt(0)
	v_mfma_f32_32x32x16_bf16 v[64:79], v[166:169], v[130:133], v[64:79]
	s_min_i32 s2, s39, s14
	s_mul_i32 s2, s2, s62
	s_lshl_b32 s72, s2, 6
	s_lshl_b64 s[2:3], s[72:73], 1
	s_add_u32 s12, s10, s2
	s_addc_u32 s13, s11, s3
	s_add_u32 s2, s8, s2
	s_addc_u32 s3, s9, s3
	global_load_dwordx4 v[162:165], v128, s[12:13]
	global_load_dwordx4 v[166:169], v198, s[12:13]
	global_load_dwordx4 v[170:173], v128, s[2:3]
	global_load_dwordx4 v[174:177], v198, s[2:3]
	ds_read_b64_tr_b16 v[80:81], v211 offset:0
	ds_read_b64_tr_b16 v[82:83], v211 offset:0x800
	ds_read_b64_tr_b16 v[84:85], v211 offset:0x1000
	ds_read_b64_tr_b16 v[86:87], v211 offset:0x1800
	ds_read_b64_tr_b16 v[88:89], v211 offset:0x2000
	ds_read_b64_tr_b16 v[90:91], v211 offset:0x2800
	ds_read_b64_tr_b16 v[92:93], v211 offset:0x3000
	ds_read_b64_tr_b16 v[94:95], v211 offset:0x3800
	s_waitcnt lgkmcnt(0)
	s_nop 0
	v_mfma_f32_32x32x16_bf16 v[0:15], v[80:83], v[124:127], v[0:15]
	v_mfma_f32_32x32x16_bf16 v[0:15], v[84:87], v[120:123], v[0:15]
	v_mfma_f32_32x32x16_bf16 v[0:15], v[88:91], v[112:115], v[0:15]
	ds_read_b64_tr_b16 v[80:81], v211 offset:0x200
	ds_read_b64_tr_b16 v[82:83], v211 offset:0xa00
	ds_read_b64_tr_b16 v[84:85], v211 offset:0x1200
	v_mfma_f32_32x32x16_bf16 v[0:15], v[92:95], v[116:119], v[0:15]
	ds_read_b64_tr_b16 v[86:87], v211 offset:0x1a00
	ds_read_b64_tr_b16 v[88:89], v211 offset:0x2200
	ds_read_b64_tr_b16 v[90:91], v211 offset:0x2a00
	ds_read_b64_tr_b16 v[92:93], v211 offset:0x3200
	ds_read_b64_tr_b16 v[94:95], v211 offset:0x3a00
	s_waitcnt lgkmcnt(0)
	v_mfma_f32_32x32x16_bf16 v[48:63], v[80:83], v[124:127], v[48:63]
	v_mfma_f32_32x32x16_bf16 v[48:63], v[84:87], v[120:123], v[48:63]
	v_mfma_f32_32x32x16_bf16 v[48:63], v[88:91], v[112:115], v[48:63]
	ds_read_b64_tr_b16 v[80:81], v211 offset:0x400
	ds_read_b64_tr_b16 v[82:83], v211 offset:0xc00
	ds_read_b64_tr_b16 v[84:85], v211 offset:0x1400
	ds_read_b64_tr_b16 v[86:87], v211 offset:0x1c00
	v_mfma_f32_32x32x16_bf16 v[48:63], v[92:95], v[116:119], v[48:63]
	ds_read_b64_tr_b16 v[88:89], v211 offset:0x2400
	ds_read_b64_tr_b16 v[90:91], v211 offset:0x2c00
	ds_read_b64_tr_b16 v[92:93], v211 offset:0x3400
	ds_read_b64_tr_b16 v[94:95], v211 offset:0x3c00
	s_waitcnt lgkmcnt(0)
	v_mfma_f32_32x32x16_bf16 v[32:47], v[80:83], v[124:127], v[32:47]
	v_exp_f32_e32 v80, v64
	v_exp_f32_e32 v81, v65
	v_exp_f32_e32 v64, v96
	v_exp_f32_e32 v65, v97
	v_exp_f32_e32 v82, v66
	v_exp_f32_e32 v83, v67
	v_exp_f32_e32 v66, v98
	v_exp_f32_e32 v67, v99
	v_mfma_f32_32x32x16_bf16 v[32:47], v[84:87], v[120:123], v[32:47]
	v_exp_f32_e32 v84, v68
	v_exp_f32_e32 v85, v69
	v_exp_f32_e32 v68, v100
	v_exp_f32_e32 v69, v101
	v_exp_f32_e32 v86, v70
	v_exp_f32_e32 v87, v71
	v_exp_f32_e32 v70, v102
	v_exp_f32_e32 v71, v103
	v_mfma_f32_32x32x16_bf16 v[32:47], v[88:91], v[112:115], v[32:47]
	v_exp_f32_e32 v194, v72
	v_exp_f32_e32 v195, v73
	ds_read_b64_tr_b16 v[72:73], v211 offset:0x600
	v_exp_f32_e32 v196, v74
	v_exp_f32_e32 v197, v75
	ds_read_b64_tr_b16 v[74:75], v211 offset:0xe00
	v_mfma_f32_32x32x16_bf16 v[32:47], v[92:95], v[116:119], v[32:47]
	v_exp_f32_e32 v92, v76
	v_exp_f32_e32 v93, v77
	ds_read_b64_tr_b16 v[76:77], v211 offset:0x1600
	v_exp_f32_e32 v94, v78
	v_exp_f32_e32 v95, v79
	ds_read_b64_tr_b16 v[78:79], v211 offset:0x1e00
	ds_read_b64_tr_b16 v[96:97], v211 offset:0x2600
	ds_read_b64_tr_b16 v[98:99], v211 offset:0x2e00
	ds_read_b64_tr_b16 v[100:101], v211 offset:0x3600
	ds_read_b64_tr_b16 v[102:103], v211 offset:0x3e00
	s_waitcnt lgkmcnt(0)
	v_mfma_f32_32x32x16_bf16 v[16:31], v[72:75], v[124:127], v[16:31]
	v_exp_f32_e32 v72, v104
	v_exp_f32_e32 v73, v105
	v_exp_f32_e32 v74, v106
	v_exp_f32_e32 v75, v107
	v_mfma_f32_32x32x16_bf16 v[16:31], v[76:79], v[120:123], v[16:31]
	v_exp_f32_e32 v76, v108
	v_exp_f32_e32 v77, v109
	v_exp_f32_e32 v78, v110
	v_exp_f32_e32 v79, v111
	s_barrier
	v_mfma_f32_32x32x16_bf16 v[16:31], v[96:99], v[112:115], v[16:31]
	s_waitcnt vmcnt(4)
	s_waitcnt vmcnt(7)
	ds_write_b128 v212, v[178:181] offset:16384
	s_waitcnt vmcnt(6)
	ds_write_b128 v213, v[182:185] offset:16384
	s_waitcnt vmcnt(5)
	ds_write_b128 v214, v[186:189] offset:49152
	s_waitcnt vmcnt(4)
	ds_write_b128 v215, v[190:193] offset:49152
	v_mfma_f32_32x32x16_bf16 v[16:31], v[100:103], v[116:119], v[16:31]
